# M1/M2 K loops: first two counted waits of a follow-on unit skipped (tiles already retired by epilogue vmcnt(0)); M2 unit-header vmcnt(0) removed so result stores drain under the first MFMA segments
# speedup vs baseline: 1.0117x; 1.0032x over previous
_ZN2mk4megaENS_4ArgsE:
	s_mov_b32 s100, 0
	s_load_dwordx4 s[88:91], s[0:1], 0x100
	s_load_dwordx2 s[4:5], s[0:1], 0x110
	v_cmp_gt_u32_e32 vcc, 64, v0
	s_waitcnt lgkmcnt(0)
	v_writelane_b32 v251, s4, 0
	s_nop 1
	v_writelane_b32 v251, s5, 1
	s_and_saveexec_b64 s[4:5], vcc
	v_lshl_add_u32 v1, v0, 2, 0
	v_add_u32_e32 v1, 0x23400, v1
	v_mov_b32_e32 v2, 0
	ds_write_b32 v1, v2
	s_or_b64 exec, exec, s[4:5]
	s_load_dwordx2 s[4:5], s[0:1], 0x110
	s_add_u32 s12, s90, 0x1000
	s_addc_u32 s13, s91, 0
	s_mov_b32 s33, 0
	s_waitcnt lgkmcnt(0)
	s_sub_i32 s3, s5, s4
	s_cmp_lt_i32 s3, 2
	s_mov_b32 s3, 0
	v_writelane_b32 v251, s3, 2
	s_barrier
	s_cbranch_scc1 .LBB0_7
	s_getreg_b32 s3, hwreg(HW_REG_XCC_ID, 0, 4)
	s_and_b32 s33, s3, 15
	v_cmp_eq_u32_e32 vcc, 0, v0
	s_and_saveexec_b64 s[4:5], vcc
	s_cbranch_execz .LBB0_6
	s_mov_b64 s[6:7], exec
	v_mbcnt_lo_u32_b32 v1, s6, 0
	v_mbcnt_hi_u32_b32 v1, s7, v1
	v_cmp_eq_u32_e32 vcc, 0, v1
	s_and_b64 s[8:9], exec, vcc
	s_mov_b64 exec, s[8:9]
	s_cbranch_execz .LBB0_6
	s_lshl_b32 s3, s33, 8
	s_bcnt1_i32_b64 s6, s[6:7]
	v_mov_b32_e32 v1, s3
	v_mov_b32_e32 v2, s6
	global_atomic_add v1, v2, s[12:13] offset:1024

.LBB0_2836:
	s_andn2_b64 vcc, exec, s[38:39]
	v_mov_b32_e32 v136, s18
	v_mov_b32_e32 v64, v175
	v_mov_b32_e32 v60, v173
	v_mov_b32_e32 v62, v174
	v_mov_b32_e32 v58, v172
	s_mov_b64 s[38:39], s[36:37]
	v_mov_b64_e32 v[138:139], v[4:5]
	s_cbranch_vccz .LBB0_2848
	s_mov_b32 s100, 1

.LBB0_2842:
	s_add_u32 s40, s38, 0x100
	s_addc_u32 s41, s39, 0
	s_add_u32 s22, s52, s38
	s_addc_u32 s28, s53, s39
	s_cmpk_eq_i32 s38, 0x700
	s_cselect_b64 vcc, -1, 0
	s_and_b64 s[42:43], vcc, exec
	s_cselect_b32 s55, 0, s40
	s_cselect_b32 s43, s31, s28
	s_cselect_b32 s42, s51, s22
	s_add_i32 s22, 0, 0x10000
	v_add_u32_e32 v59, s22, v169
	s_add_i32 s28, 0, 0x14000
	ds_read_b128 v[76:79], v59
	ds_read_b128 v[176:179], v59 offset:1024
	ds_read_b128 v[184:187], v59 offset:2048
	ds_read_b128 v[188:191], v59 offset:3072
	v_add_u32_e32 v59, s28, v169
	ds_read_b128 v[192:195], v59
	ds_read_b128 v[196:199], v59 offset:1024
	ds_read_b128 v[200:203], v59 offset:2048
	ds_read_b128 v[204:207], v59 offset:3072
	v_lshl_add_u64 v[80:81], v[74:75], 0, s[38:39]
	s_add_i32 m0, s27, 0xc000
	ds_read_b128 v[208:211], v171
	ds_read_b128 v[226:229], v171 offset:1024
	ds_read_b128 v[230:233], v171 offset:2048
	ds_read_b128 v[234:237], v171 offset:3072
	ds_read_b128 v[238:241], v171 offset:4096
	ds_read_b128 v[242:245], v171 offset:5120
	ds_read_b128 v[246:249], v171 offset:6144
	ds_read_b128 v[218:221], v171 offset:7168
	global_load_lds_dwordx4 v[80:81], off
	v_lshl_add_u64 v[80:81], v[2:3], 0, s[38:39]
	s_add_i32 m0, s27, 0xe000
	s_nop 0
	global_load_lds_dwordx4 v[80:81], off
	s_cmp_lg_u32 s100, 0
	s_cbranch_scc1 .Lrelaxw_m1_0
	s_waitcnt vmcnt(8)
.Lrelaxw_m1_0:
	s_waitcnt lgkmcnt(0)
	s_barrier
	s_setprio 1
	s_waitcnt lgkmcnt(0)
	v_mfma_f32_16x16x32_bf16 v[152:155], v[76:79], v[208:211], v[152:155]
	v_mfma_f32_16x16x32_bf16 v[144:147], v[184:187], v[208:211], v[144:147]
	v_mfma_f32_16x16x32_bf16 v[132:135], v[76:79], v[230:233], v[132:135]
	v_mfma_f32_16x16x32_bf16 v[124:127], v[184:187], v[230:233], v[124:127]
	v_mfma_f32_16x16x32_bf16 v[116:119], v[76:79], v[238:241], v[116:119]
	v_mfma_f32_16x16x32_bf16 v[108:111], v[184:187], v[238:241], v[108:111]
	v_mfma_f32_16x16x32_bf16 v[100:103], v[76:79], v[246:249], v[100:103]
	v_mfma_f32_16x16x32_bf16 v[90:93], v[184:187], v[246:249], v[90:93]
	v_mfma_f32_16x16x32_bf16 v[152:155], v[176:179], v[226:229], v[152:155]
	v_mfma_f32_16x16x32_bf16 v[144:147], v[188:191], v[226:229], v[144:147]
	v_mfma_f32_16x16x32_bf16 v[132:135], v[176:179], v[234:237], v[132:135]
	v_mfma_f32_16x16x32_bf16 v[124:127], v[188:191], v[234:237], v[124:127]
	v_mfma_f32_16x16x32_bf16 v[116:119], v[176:179], v[242:245], v[116:119]
	v_mfma_f32_16x16x32_bf16 v[108:111], v[188:191], v[242:245], v[108:111]
	v_mfma_f32_16x16x32_bf16 v[100:103], v[176:179], v[218:221], v[100:103]
	v_mfma_f32_16x16x32_bf16 v[90:93], v[188:191], v[218:221], v[90:93]
	s_setprio 0
	s_setprio 1
	v_mfma_f32_16x16x32_bf16 v[148:151], v[192:195], v[208:211], v[148:151]
	v_mfma_f32_16x16x32_bf16 v[140:143], v[200:203], v[208:211], v[140:143]
	v_mfma_f32_16x16x32_bf16 v[128:131], v[192:195], v[230:233], v[128:131]
	v_mfma_f32_16x16x32_bf16 v[120:123], v[200:203], v[230:233], v[120:123]
	v_mfma_f32_16x16x32_bf16 v[112:115], v[192:195], v[238:241], v[112:115]
	v_mfma_f32_16x16x32_bf16 v[104:107], v[200:203], v[238:241], v[104:107]
	v_mfma_f32_16x16x32_bf16 v[94:97], v[192:195], v[246:249], v[94:97]
	v_mfma_f32_16x16x32_bf16 v[86:89], v[200:203], v[246:249], v[86:89]
	v_mfma_f32_16x16x32_bf16 v[148:151], v[196:199], v[226:229], v[148:151]
	v_mfma_f32_16x16x32_bf16 v[140:143], v[204:207], v[226:229], v[140:143]
	v_mfma_f32_16x16x32_bf16 v[128:131], v[196:199], v[234:237], v[128:131]
	v_mfma_f32_16x16x32_bf16 v[120:123], v[204:207], v[234:237], v[120:123]
	v_mfma_f32_16x16x32_bf16 v[112:115], v[196:199], v[242:245], v[112:115]
	v_mfma_f32_16x16x32_bf16 v[104:107], v[204:207], v[242:245], v[104:107]
	v_mfma_f32_16x16x32_bf16 v[94:97], v[196:199], v[218:221], v[94:97]
	v_mfma_f32_16x16x32_bf16 v[86:89], v[204:207], v[218:221], v[86:89]
	s_setprio 0
	s_barrier
	s_add_i32 s22, s22, s24
	v_lshl_add_u64 v[160:161], s[42:43], 0, v[158:159]
	s_mov_b32 m0, s22
	ds_read_b128 v[208:211], v171 offset:16384
	ds_read_b128 v[218:221], v171 offset:17408
	ds_read_b128 v[226:229], v171 offset:18432
	ds_read_b128 v[230:233], v171 offset:19456
	ds_read_b128 v[234:237], v171 offset:20480
	ds_read_b128 v[238:241], v171 offset:21504
	ds_read_b128 v[242:245], v171 offset:22528
	ds_read_b128 v[246:249], v171 offset:23552
	global_load_lds_dwordx4 v[160:161], off
	s_add_i32 m0, s22, 0x2000
	s_add_u32 s38, s42, 0x40000
	v_lshl_add_u64 v[180:181], s[42:43], 0, v[156:157]
	s_addc_u32 s39, s43, 0
	s_add_i32 s22, s28, s24
	global_load_lds_dwordx4 v[180:181], off
	v_lshl_add_u64 v[80:81], s[38:39], 0, v[158:159]
	s_mov_b32 m0, s22
	v_cndmask_b32_e32 v98, v58, v172, vcc
	global_load_lds_dwordx4 v[80:81], off
	s_add_i32 m0, s22, 0x2000
	v_lshl_add_u64 v[80:81], s[38:39], 0, v[156:157]
	s_add_u32 s38, s6, s55
	global_load_lds_dwordx4 v[80:81], off
	s_addc_u32 s39, s7, 0
	s_mov_b32 m0, s27
	v_cndmask_b32_e32 v80, v62, v174, vcc
	global_load_lds_dwordx4 v98, s[38:39]
	s_mov_b32 m0, s44
	v_mov_b32_e32 v81, v99
	global_load_lds_dwordx4 v80, s[38:39]
	s_cmp_lg_u32 s100, 0
	s_cbranch_scc1 .Lrelaxw_m1_1
	s_waitcnt vmcnt(8)
.Lrelaxw_m1_1:
	s_waitcnt lgkmcnt(0)
	v_lshl_add_u64 v[182:183], s[38:39], 0, v[98:99]
	v_lshl_add_u64 v[212:213], s[38:39], 0, v[80:81]
	s_barrier
	s_setprio 1
	s_waitcnt lgkmcnt(0)
	v_mfma_f32_16x16x32_bf16 v[70:73], v[76:79], v[208:211], v[70:73]
	v_mfma_f32_16x16x32_bf16 v[54:57], v[184:187], v[208:211], v[54:57]
	v_mfma_f32_16x16x32_bf16 v[46:49], v[76:79], v[226:229], v[46:49]
	v_mfma_f32_16x16x32_bf16 v[38:41], v[184:187], v[226:229], v[38:41]
	v_mfma_f32_16x16x32_bf16 v[30:33], v[76:79], v[234:237], v[30:33]
	v_mfma_f32_16x16x32_bf16 v[22:25], v[184:187], v[234:237], v[22:25]
	v_mfma_f32_16x16x32_bf16 v[14:17], v[76:79], v[242:245], v[14:17]
	v_mfma_f32_16x16x32_bf16 v[6:9], v[184:187], v[242:245], v[6:9]
	v_mfma_f32_16x16x32_bf16 v[70:73], v[176:179], v[218:221], v[70:73]
	v_mfma_f32_16x16x32_bf16 v[54:57], v[188:191], v[218:221], v[54:57]
	v_mfma_f32_16x16x32_bf16 v[46:49], v[176:179], v[230:233], v[46:49]
	v_mfma_f32_16x16x32_bf16 v[38:41], v[188:191], v[230:233], v[38:41]
	v_mfma_f32_16x16x32_bf16 v[30:33], v[176:179], v[238:241], v[30:33]
	v_mfma_f32_16x16x32_bf16 v[22:25], v[188:191], v[238:241], v[22:25]
	v_mfma_f32_16x16x32_bf16 v[14:17], v[176:179], v[246:249], v[14:17]
	v_mfma_f32_16x16x32_bf16 v[6:9], v[188:191], v[246:249], v[6:9]
	s_setprio 0
	s_setprio 1
	v_mfma_f32_16x16x32_bf16 v[66:69], v[200:203], v[208:211], v[66:69]
	v_mfma_f32_16x16x32_bf16 v[50:53], v[192:195], v[226:229], v[50:53]
	v_mfma_f32_16x16x32_bf16 v[42:45], v[200:203], v[226:229], v[42:45]
	v_mfma_f32_16x16x32_bf16 v[34:37], v[192:195], v[234:237], v[34:37]
	v_mfma_f32_16x16x32_bf16 v[26:29], v[200:203], v[234:237], v[26:29]
	v_mfma_f32_16x16x32_bf16 v[18:21], v[192:195], v[242:245], v[18:21]
	v_mfma_f32_16x16x32_bf16 v[10:13], v[200:203], v[242:245], v[10:13]
	v_mfma_f32_16x16x32_bf16 v[76:79], v[192:195], v[208:211], v[82:85]
	v_mfma_f32_16x16x32_bf16 v[66:69], v[204:207], v[218:221], v[66:69]
	v_mfma_f32_16x16x32_bf16 v[50:53], v[196:199], v[230:233], v[50:53]
	v_mfma_f32_16x16x32_bf16 v[42:45], v[204:207], v[230:233], v[42:45]
	v_mfma_f32_16x16x32_bf16 v[34:37], v[196:199], v[238:241], v[34:37]
	v_mfma_f32_16x16x32_bf16 v[26:29], v[204:207], v[238:241], v[26:29]
	v_mfma_f32_16x16x32_bf16 v[18:21], v[196:199], v[246:249], v[18:21]
	v_mfma_f32_16x16x32_bf16 v[10:13], v[204:207], v[246:249], v[10:13]
	v_mfma_f32_16x16x32_bf16 v[76:79], v[196:199], v[218:221], v[76:79]
	s_setprio 0
	s_barrier
	s_add_i32 s22, 0, 0x18000
	v_add_u32_e32 v59, s22, v169
	s_add_i32 s28, 0, 0x1c000
	ds_read_b128 v[80:83], v59
	ds_read_b128 v[176:179], v59 offset:1024
	ds_read_b128 v[184:187], v59 offset:2048
	ds_read_b128 v[188:191], v59 offset:3072
	v_add_u32_e32 v59, s28, v169
	ds_read_b128 v[192:195], v59
	ds_read_b128 v[196:199], v59 offset:1024
	ds_read_b128 v[200:203], v59 offset:2048
	ds_read_b128 v[204:207], v59 offset:3072
	s_mov_b32 m0, s45
	v_cndmask_b32_e32 v59, v60, v173, vcc
	ds_read_b128 v[208:211], v171 offset:32768
	ds_read_b128 v[218:221], v171 offset:33792
	ds_read_b128 v[226:229], v171 offset:34816
	ds_read_b128 v[230:233], v171 offset:35840
	ds_read_b128 v[234:237], v171 offset:36864
	ds_read_b128 v[238:241], v171 offset:37888
	ds_read_b128 v[242:245], v171 offset:38912
	ds_read_b128 v[246:249], v171 offset:39936
	v_cndmask_b32_e32 v61, v64, v175, vcc
	global_load_lds_dwordx4 v59, s[38:39]
	s_mov_b32 m0, s46
	s_nop 0
	global_load_lds_dwordx4 v61, s[38:39]
	s_waitcnt vmcnt(8)
	s_waitcnt lgkmcnt(0)
	s_barrier
	s_setprio 1
	s_waitcnt lgkmcnt(0)
	v_mfma_f32_16x16x32_bf16 v[152:155], v[80:83], v[208:211], v[152:155]
	v_mfma_f32_16x16x32_bf16 v[144:147], v[184:187], v[208:211], v[144:147]
	v_mfma_f32_16x16x32_bf16 v[132:135], v[80:83], v[226:229], v[132:135]
	v_mfma_f32_16x16x32_bf16 v[124:127], v[184:187], v[226:229], v[124:127]
	v_mfma_f32_16x16x32_bf16 v[116:119], v[80:83], v[234:237], v[116:119]
	v_mfma_f32_16x16x32_bf16 v[108:111], v[184:187], v[234:237], v[108:111]
	v_mfma_f32_16x16x32_bf16 v[100:103], v[80:83], v[242:245], v[100:103]
	v_mfma_f32_16x16x32_bf16 v[90:93], v[184:187], v[242:245], v[90:93]
	v_mfma_f32_16x16x32_bf16 v[152:155], v[176:179], v[218:221], v[152:155]
	v_mfma_f32_16x16x32_bf16 v[144:147], v[188:191], v[218:221], v[144:147]
	v_mfma_f32_16x16x32_bf16 v[132:135], v[176:179], v[230:233], v[132:135]
	v_mfma_f32_16x16x32_bf16 v[124:127], v[188:191], v[230:233], v[124:127]
	v_mfma_f32_16x16x32_bf16 v[116:119], v[176:179], v[238:241], v[116:119]
	v_mfma_f32_16x16x32_bf16 v[108:111], v[188:191], v[238:241], v[108:111]
	v_mfma_f32_16x16x32_bf16 v[100:103], v[176:179], v[246:249], v[100:103]
	v_mfma_f32_16x16x32_bf16 v[90:93], v[188:191], v[246:249], v[90:93]
	s_setprio 0
	s_setprio 1
	v_mfma_f32_16x16x32_bf16 v[148:151], v[192:195], v[208:211], v[148:151]
	v_mfma_f32_16x16x32_bf16 v[140:143], v[200:203], v[208:211], v[140:143]
	v_mfma_f32_16x16x32_bf16 v[128:131], v[192:195], v[226:229], v[128:131]
	v_mfma_f32_16x16x32_bf16 v[120:123], v[200:203], v[226:229], v[120:123]
	v_mfma_f32_16x16x32_bf16 v[112:115], v[192:195], v[234:237], v[112:115]
	v_mfma_f32_16x16x32_bf16 v[104:107], v[200:203], v[234:237], v[104:107]
	v_mfma_f32_16x16x32_bf16 v[94:97], v[192:195], v[242:245], v[94:97]
	v_mfma_f32_16x16x32_bf16 v[84:87], v[200:203], v[242:245], v[86:89]
	v_mfma_f32_16x16x32_bf16 v[148:151], v[196:199], v[218:221], v[148:151]
	v_mfma_f32_16x16x32_bf16 v[140:143], v[204:207], v[218:221], v[140:143]
	v_mfma_f32_16x16x32_bf16 v[128:131], v[196:199], v[230:233], v[128:131]
	v_mfma_f32_16x16x32_bf16 v[120:123], v[204:207], v[230:233], v[120:123]
	v_mfma_f32_16x16x32_bf16 v[112:115], v[196:199], v[238:241], v[112:115]
	v_mfma_f32_16x16x32_bf16 v[104:107], v[204:207], v[238:241], v[104:107]
	v_mfma_f32_16x16x32_bf16 v[94:97], v[196:199], v[246:249], v[94:97]
	v_mfma_f32_16x16x32_bf16 v[86:89], v[204:207], v[246:249], v[84:87]
	s_setprio 0
	s_barrier
	s_add_i32 s22, s22, s24
	v_lshl_add_u64 v[84:85], v[160:161], 0, s[0:1]
	s_mov_b32 m0, s22
	ds_read_b128 v[208:211], v171 offset:49152
	ds_read_b128 v[218:221], v171 offset:50176
	ds_read_b128 v[226:229], v171 offset:51200
	ds_read_b128 v[230:233], v171 offset:52224
	ds_read_b128 v[234:237], v171 offset:53248
	ds_read_b128 v[238:241], v171 offset:54272
	ds_read_b128 v[242:245], v171 offset:55296
	ds_read_b128 v[246:249], v171 offset:56320
	global_load_lds_dwordx4 v[84:85], off
	s_add_i32 m0, s22, 0x2000
	s_add_u32 s38, s42, 0x40080
	v_lshl_add_u64 v[84:85], v[180:181], 0, s[0:1]
	s_addc_u32 s39, s43, 0
	s_add_i32 s22, s28, s24
	global_load_lds_dwordx4 v[84:85], off
	v_lshl_add_u64 v[84:85], s[38:39], 0, v[158:159]
	s_mov_b32 m0, s22
	s_nop 0
	global_load_lds_dwordx4 v[84:85], off
	v_lshl_add_u64 v[84:85], s[38:39], 0, v[156:157]
	s_add_i32 m0, s22, 0x2000
	s_nop 0
	global_load_lds_dwordx4 v[84:85], off
	v_lshl_add_u64 v[84:85], v[182:183], 0, s[0:1]
	s_mov_b32 m0, s4
	s_nop 0
	global_load_lds_dwordx4 v[84:85], off
	v_lshl_add_u64 v[84:85], v[212:213], 0, s[0:1]
	s_mov_b32 m0, s47
	s_nop 0
	global_load_lds_dwordx4 v[84:85], off
	s_waitcnt vmcnt(8)
	s_waitcnt lgkmcnt(0)
	s_barrier
	s_setprio 1
	s_waitcnt lgkmcnt(0)
	v_mfma_f32_16x16x32_bf16 v[70:73], v[80:83], v[208:211], v[70:73]
	v_mfma_f32_16x16x32_bf16 v[54:57], v[184:187], v[208:211], v[54:57]
	v_mfma_f32_16x16x32_bf16 v[46:49], v[80:83], v[226:229], v[46:49]
	v_mfma_f32_16x16x32_bf16 v[38:41], v[184:187], v[226:229], v[38:41]
	v_mfma_f32_16x16x32_bf16 v[30:33], v[80:83], v[234:237], v[30:33]
	v_mfma_f32_16x16x32_bf16 v[22:25], v[184:187], v[234:237], v[22:25]
	v_mfma_f32_16x16x32_bf16 v[14:17], v[80:83], v[242:245], v[14:17]
	v_mfma_f32_16x16x32_bf16 v[6:9], v[184:187], v[242:245], v[6:9]
	v_mfma_f32_16x16x32_bf16 v[70:73], v[176:179], v[218:221], v[70:73]
	v_mfma_f32_16x16x32_bf16 v[54:57], v[188:191], v[218:221], v[54:57]
	v_mfma_f32_16x16x32_bf16 v[46:49], v[176:179], v[230:233], v[46:49]
	v_mfma_f32_16x16x32_bf16 v[38:41], v[188:191], v[230:233], v[38:41]
	v_mfma_f32_16x16x32_bf16 v[30:33], v[176:179], v[238:241], v[30:33]
	v_mfma_f32_16x16x32_bf16 v[22:25], v[188:191], v[238:241], v[22:25]
	v_mfma_f32_16x16x32_bf16 v[14:17], v[176:179], v[246:249], v[14:17]
	v_mfma_f32_16x16x32_bf16 v[6:9], v[188:191], v[246:249], v[6:9]
	s_setprio 0
	s_setprio 1
	v_mfma_f32_16x16x32_bf16 v[76:79], v[192:195], v[208:211], v[76:79]
	v_mfma_f32_16x16x32_bf16 v[66:69], v[200:203], v[208:211], v[66:69]
	v_mfma_f32_16x16x32_bf16 v[50:53], v[192:195], v[226:229], v[50:53]
	v_mfma_f32_16x16x32_bf16 v[42:45], v[200:203], v[226:229], v[42:45]
	v_mfma_f32_16x16x32_bf16 v[34:37], v[192:195], v[234:237], v[34:37]
	v_mfma_f32_16x16x32_bf16 v[26:29], v[200:203], v[234:237], v[26:29]
	v_mfma_f32_16x16x32_bf16 v[18:21], v[192:195], v[242:245], v[18:21]
	v_mfma_f32_16x16x32_bf16 v[10:13], v[200:203], v[242:245], v[10:13]
	v_mfma_f32_16x16x32_bf16 v[82:85], v[196:199], v[218:221], v[76:79]
	v_mfma_f32_16x16x32_bf16 v[66:69], v[204:207], v[218:221], v[66:69]
	v_mfma_f32_16x16x32_bf16 v[50:53], v[196:199], v[230:233], v[50:53]
	v_mfma_f32_16x16x32_bf16 v[42:45], v[204:207], v[230:233], v[42:45]
	v_mfma_f32_16x16x32_bf16 v[34:37], v[196:199], v[238:241], v[34:37]
	v_mfma_f32_16x16x32_bf16 v[26:29], v[204:207], v[238:241], v[26:29]
	v_mfma_f32_16x16x32_bf16 v[18:21], v[196:199], v[246:249], v[18:21]
	v_mfma_f32_16x16x32_bf16 v[10:13], v[204:207], v[246:249], v[10:13]
	s_setprio 0
	s_barrier
	s_mov_b32 s100, 0
	s_add_i32 s54, s54, 2
	s_cmp_gt_u32 s54, 13
	s_mov_b64 s[38:39], s[40:41]
	s_cbranch_scc0 .LBB0_2842
	s_and_b64 vcc, exec, s[14:15]
	s_cbranch_vccz .LBB0_2845
	s_barrier

.LBB0_2954:
	s_andn2_b64 vcc, exec, s[18:19]
	s_mov_b32 s31, s56
	s_mov_b64 s[40:41], s[36:37]
	s_mov_b64 s[38:39], s[34:35]
	v_mov_b64_e32 v[22:23], v[4:5]
	s_cbranch_vccz .LBB0_2980
	s_mov_b32 s100, 1

.LBB0_2957:
	s_ashr_i32 s35, s16, 31
	s_mov_b32 s34, s16
	s_lshl_b64 s[34:35], s[34:35], 19
	s_add_u32 s34, s27, s34
	s_addc_u32 s35, s49, s35
	s_ashr_i32 s37, s17, 31
	s_mov_b32 s36, s17
	s_lshl_b64 s[36:37], s[36:37], 19
	s_add_u32 s36, s25, s36
	s_addc_u32 s37, s26, s37
	s_and_b64 s[42:43], s[18:19], exec
	s_cselect_b32 s57, s37, s41
	s_cselect_b32 s64, s36, s40
	s_add_u32 s65, s40, 0x100
	s_addc_u32 s76, s41, 0
	s_add_u32 s40, s38, 0x40080
	s_addc_u32 s41, s39, 0
	v_mov_b32_e32 v6, 0
	v_lshl_add_u64 v[2:3], s[40:41], 0, v[158:159]
	v_lshl_add_u64 v[140:141], s[40:41], 0, v[160:161]
	s_mov_b32 s78, -2
	s_mov_b64 s[40:41], 0
	v_mov_b32_e32 v7, v6
	v_mov_b32_e32 v8, v6
	v_mov_b32_e32 v9, v6
	v_mov_b32_e32 v10, v6
	v_mov_b32_e32 v11, v6
	v_mov_b32_e32 v12, v6
	v_mov_b32_e32 v13, v6
	v_mov_b32_e32 v24, v6
	v_mov_b32_e32 v25, v6
	v_mov_b32_e32 v26, v6
	v_mov_b32_e32 v27, v6
	v_mov_b32_e32 v28, v6
	v_mov_b32_e32 v29, v6
	v_mov_b32_e32 v30, v6
	v_mov_b32_e32 v31, v6
	v_mov_b32_e32 v40, v6
	v_mov_b32_e32 v41, v6
	v_mov_b32_e32 v42, v6
	v_mov_b32_e32 v43, v6
	v_mov_b32_e32 v44, v6
	v_mov_b32_e32 v45, v6
	v_mov_b32_e32 v46, v6
	v_mov_b32_e32 v47, v6
	v_mov_b32_e32 v56, v6
	v_mov_b32_e32 v57, v6
	v_mov_b32_e32 v58, v6
	v_mov_b32_e32 v59, v6
	v_mov_b32_e32 v60, v6
	v_mov_b32_e32 v61, v6
	v_mov_b32_e32 v62, v6
	v_mov_b32_e32 v63, v6
	v_mov_b32_e32 v14, v6
	v_mov_b32_e32 v15, v6
	v_mov_b32_e32 v16, v6
	v_mov_b32_e32 v17, v6
	v_mov_b32_e32 v18, v6
	v_mov_b32_e32 v19, v6
	v_mov_b32_e32 v20, v6
	v_mov_b32_e32 v21, v6
	v_mov_b32_e32 v32, v6
	v_mov_b32_e32 v33, v6
	v_mov_b32_e32 v34, v6
	v_mov_b32_e32 v35, v6
	v_mov_b32_e32 v36, v6
	v_mov_b32_e32 v37, v6
	v_mov_b32_e32 v38, v6
	v_mov_b32_e32 v39, v6
	v_mov_b32_e32 v48, v6
	v_mov_b32_e32 v49, v6
	v_mov_b32_e32 v50, v6
	v_mov_b32_e32 v51, v6
	v_mov_b32_e32 v52, v6
	v_mov_b32_e32 v53, v6
	v_mov_b32_e32 v54, v6
	v_mov_b32_e32 v55, v6
	v_mov_b32_e32 v64, v6
	v_mov_b32_e32 v65, v6
	v_mov_b32_e32 v66, v6
	v_mov_b32_e32 v67, v6
	v_mov_b32_e32 v68, v6
	v_mov_b32_e32 v69, v6
	v_mov_b32_e32 v70, v6
	v_mov_b32_e32 v71, v6
	v_mov_b32_e32 v72, v6
	v_mov_b32_e32 v73, v6
	v_mov_b32_e32 v74, v6
	v_mov_b32_e32 v75, v6
	v_mov_b32_e32 v76, v6
	v_mov_b32_e32 v77, v6
	v_mov_b32_e32 v78, v6
	v_mov_b32_e32 v79, v6
	v_mov_b32_e32 v88, v6
	v_mov_b32_e32 v89, v6
	v_mov_b32_e32 v90, v6
	v_mov_b32_e32 v91, v6
	v_mov_b32_e32 v92, v6
	v_mov_b32_e32 v93, v6
	v_mov_b32_e32 v94, v6
	v_mov_b32_e32 v95, v6
	v_mov_b32_e32 v108, v6
	v_mov_b32_e32 v109, v6
	v_mov_b32_e32 v110, v6
	v_mov_b32_e32 v111, v6
	v_mov_b32_e32 v112, v6
	v_mov_b32_e32 v113, v6
	v_mov_b32_e32 v114, v6
	v_mov_b32_e32 v115, v6
	v_mov_b32_e32 v124, v6
	v_mov_b32_e32 v125, v6
	v_mov_b32_e32 v126, v6
	v_mov_b32_e32 v127, v6
	v_mov_b32_e32 v128, v6
	v_mov_b32_e32 v129, v6
	v_mov_b32_e32 v130, v6
	v_mov_b32_e32 v131, v6
	v_mov_b32_e32 v80, v6
	v_mov_b32_e32 v81, v6
	v_mov_b32_e32 v82, v6
	v_mov_b32_e32 v83, v6
	v_mov_b32_e32 v84, v6
	v_mov_b32_e32 v85, v6
	v_mov_b32_e32 v86, v6
	v_mov_b32_e32 v87, v6
	v_mov_b32_e32 v100, v6
	v_mov_b32_e32 v101, v6
	v_mov_b32_e32 v102, v6
	v_mov_b32_e32 v103, v6
	v_mov_b32_e32 v104, v6
	v_mov_b32_e32 v105, v6
	v_mov_b32_e32 v106, v6
	v_mov_b32_e32 v107, v6
	v_mov_b32_e32 v116, v6
	v_mov_b32_e32 v117, v6
	v_mov_b32_e32 v118, v6
	v_mov_b32_e32 v119, v6
	v_mov_b32_e32 v120, v6
	v_mov_b32_e32 v121, v6
	v_mov_b32_e32 v122, v6
	v_mov_b32_e32 v123, v6
	v_mov_b32_e32 v132, v6
	v_mov_b32_e32 v133, v6
	v_mov_b32_e32 v134, v6
	v_mov_b32_e32 v135, v6
	v_mov_b32_e32 v136, v6
	v_mov_b32_e32 v137, v6
	v_mov_b32_e32 v138, v6
	v_mov_b32_e32 v139, v6
.LBB0_2958:
	s_add_u32 s42, s40, 0x100
	s_addc_u32 s43, s41, 0
	s_add_u32 s22, s65, s40
	s_addc_u32 s28, s76, s41
	s_cmp_eq_u32 s78, 12
	s_cselect_b64 s[46:47], -1, 0
	s_and_b64 s[44:45], s[46:47], exec
	s_cselect_b32 s58, 0, s42
	s_cselect_b32 s45, s57, s28
	s_cselect_b32 s44, s64, s22
	s_add_i32 s22, 0, 0x10000
	v_add_u32_e32 v98, s22, v162
	s_add_i32 s28, 0, 0x14000
	ds_read_b128 v[142:145], v98
	ds_read_b128 v[146:149], v98 offset:1024
	ds_read_b128 v[150:153], v98 offset:2048
	ds_read_b128 v[166:169], v98 offset:3072
	v_add_u32_e32 v98, s28, v162
	ds_read_b128 v[170:173], v98
	ds_read_b128 v[174:177], v98 offset:1024
	ds_read_b128 v[184:187], v98 offset:2048
	ds_read_b128 v[188:191], v98 offset:3072
	v_lshl_add_u64 v[154:155], v[2:3], 0, s[40:41]
	s_add_i32 m0, s50, 0xc000
	ds_read_b128 v[192:195], v165
	ds_read_b128 v[196:199], v165 offset:1024
	ds_read_b128 v[200:203], v165 offset:2048
	ds_read_b128 v[204:207], v165 offset:3072
	ds_read_b128 v[208:211], v165 offset:4096
	ds_read_b128 v[218:221], v165 offset:5120
	ds_read_b128 v[226:229], v165 offset:6144
	ds_read_b128 v[230:233], v165 offset:7168
	global_load_lds_dwordx4 v[154:155], off
	v_lshl_add_u64 v[154:155], v[140:141], 0, s[40:41]
	s_add_i32 m0, s50, 0xe000
	s_nop 0
	global_load_lds_dwordx4 v[154:155], off
	s_cmp_lg_u32 s100, 0
	s_cbranch_scc1 .Lrelaxw_m2_0
	s_waitcnt vmcnt(8)
.Lrelaxw_m2_0:
	s_waitcnt lgkmcnt(0)
	s_barrier
	s_setprio 1
	s_waitcnt lgkmcnt(0)
	v_mfma_f32_16x16x32_bf16 v[136:139], v[142:145], v[192:195], v[136:139]
	v_mfma_f32_16x16x32_bf16 v[132:135], v[150:153], v[192:195], v[132:135]
	v_mfma_f32_16x16x32_bf16 v[120:123], v[142:145], v[200:203], v[120:123]
	v_mfma_f32_16x16x32_bf16 v[116:119], v[150:153], v[200:203], v[116:119]
	v_mfma_f32_16x16x32_bf16 v[104:107], v[142:145], v[208:211], v[104:107]
	v_mfma_f32_16x16x32_bf16 v[100:103], v[150:153], v[208:211], v[100:103]
	v_mfma_f32_16x16x32_bf16 v[84:87], v[142:145], v[226:229], v[84:87]
	v_mfma_f32_16x16x32_bf16 v[80:83], v[150:153], v[226:229], v[80:83]
	v_mfma_f32_16x16x32_bf16 v[136:139], v[146:149], v[196:199], v[136:139]
	v_mfma_f32_16x16x32_bf16 v[132:135], v[166:169], v[196:199], v[132:135]
	v_mfma_f32_16x16x32_bf16 v[120:123], v[146:149], v[204:207], v[120:123]
	v_mfma_f32_16x16x32_bf16 v[116:119], v[166:169], v[204:207], v[116:119]
	v_mfma_f32_16x16x32_bf16 v[104:107], v[146:149], v[218:221], v[104:107]
	v_mfma_f32_16x16x32_bf16 v[100:103], v[166:169], v[218:221], v[100:103]
	v_mfma_f32_16x16x32_bf16 v[84:87], v[146:149], v[230:233], v[84:87]
	v_mfma_f32_16x16x32_bf16 v[80:83], v[166:169], v[230:233], v[80:83]
	s_setprio 0
	s_setprio 1
	v_mfma_f32_16x16x32_bf16 v[128:131], v[170:173], v[192:195], v[128:131]
	v_mfma_f32_16x16x32_bf16 v[124:127], v[184:187], v[192:195], v[124:127]
	v_mfma_f32_16x16x32_bf16 v[112:115], v[170:173], v[200:203], v[112:115]
	v_mfma_f32_16x16x32_bf16 v[108:111], v[184:187], v[200:203], v[108:111]
	v_mfma_f32_16x16x32_bf16 v[92:95], v[170:173], v[208:211], v[92:95]
	v_mfma_f32_16x16x32_bf16 v[88:91], v[184:187], v[208:211], v[88:91]
	v_mfma_f32_16x16x32_bf16 v[76:79], v[170:173], v[226:229], v[76:79]
	v_mfma_f32_16x16x32_bf16 v[72:75], v[184:187], v[226:229], v[72:75]
	v_mfma_f32_16x16x32_bf16 v[128:131], v[174:177], v[196:199], v[128:131]
	v_mfma_f32_16x16x32_bf16 v[124:127], v[188:191], v[196:199], v[124:127]
	v_mfma_f32_16x16x32_bf16 v[112:115], v[174:177], v[204:207], v[112:115]
	v_mfma_f32_16x16x32_bf16 v[108:111], v[188:191], v[204:207], v[108:111]
	v_mfma_f32_16x16x32_bf16 v[92:95], v[174:177], v[218:221], v[92:95]
	v_mfma_f32_16x16x32_bf16 v[88:91], v[188:191], v[218:221], v[88:91]
	v_mfma_f32_16x16x32_bf16 v[76:79], v[174:177], v[230:233], v[76:79]
	v_mfma_f32_16x16x32_bf16 v[72:75], v[188:191], v[230:233], v[72:75]
	s_setprio 0
	s_barrier
	s_add_i32 s22, s22, s24
	v_lshl_add_u64 v[154:155], s[44:45], 0, v[96:97]
	s_mov_b32 m0, s22
	ds_read_b128 v[192:195], v165 offset:16384
	ds_read_b128 v[196:199], v165 offset:17408
	ds_read_b128 v[200:203], v165 offset:18432
	ds_read_b128 v[204:207], v165 offset:19456
	ds_read_b128 v[208:211], v165 offset:20480
	ds_read_b128 v[218:221], v165 offset:21504
	ds_read_b128 v[226:229], v165 offset:22528
	ds_read_b128 v[230:233], v165 offset:23552
	global_load_lds_dwordx4 v[154:155], off
	s_add_i32 m0, s22, 0x2000
	s_add_u32 s40, s44, 0x40000
	v_lshl_add_u64 v[178:179], s[44:45], 0, v[156:157]
	s_addc_u32 s41, s45, 0
	s_add_i32 s22, s28, s24
	global_load_lds_dwordx4 v[178:179], off
	v_lshl_add_u64 v[180:181], s[40:41], 0, v[96:97]
	s_mov_b32 m0, s22
	s_nop 0
	global_load_lds_dwordx4 v[180:181], off
	v_lshl_add_u64 v[180:181], s[40:41], 0, v[156:157]
	s_add_i32 m0, s22, 0x2000
	s_and_b64 s[40:41], s[18:19], s[46:47]
	s_and_b64 s[40:41], s[40:41], exec
	s_cselect_b32 s28, s34, s38
	s_cselect_b32 s22, s35, s39
	s_add_u32 s40, s28, s58
	s_addc_u32 s41, s22, 0
	global_load_lds_dwordx4 v[180:181], off
	v_lshl_add_u64 v[180:181], s[40:41], 0, v[96:97]
	s_mov_b32 m0, s50
	v_lshl_add_u64 v[182:183], s[40:41], 0, v[156:157]
	global_load_lds_dwordx4 v[180:181], off
	s_mov_b32 m0, s51
	s_nop 0
	global_load_lds_dwordx4 v[182:183], off
	s_cmp_lg_u32 s100, 0
	s_cbranch_scc1 .Lrelaxw_m2_1
	s_waitcnt vmcnt(8)
.Lrelaxw_m2_1:
	s_waitcnt lgkmcnt(0)
	s_barrier
	s_setprio 1
	s_waitcnt lgkmcnt(0)
	v_mfma_f32_16x16x32_bf16 v[68:71], v[142:145], v[192:195], v[68:71]
	v_mfma_f32_16x16x32_bf16 v[64:67], v[150:153], v[192:195], v[64:67]
	v_mfma_f32_16x16x32_bf16 v[52:55], v[142:145], v[200:203], v[52:55]
	v_mfma_f32_16x16x32_bf16 v[48:51], v[150:153], v[200:203], v[48:51]
	v_mfma_f32_16x16x32_bf16 v[36:39], v[142:145], v[208:211], v[36:39]
	v_mfma_f32_16x16x32_bf16 v[32:35], v[150:153], v[208:211], v[32:35]
	v_mfma_f32_16x16x32_bf16 v[18:21], v[142:145], v[226:229], v[18:21]
	v_mfma_f32_16x16x32_bf16 v[14:17], v[150:153], v[226:229], v[14:17]
	v_mfma_f32_16x16x32_bf16 v[68:71], v[146:149], v[196:199], v[68:71]
	v_mfma_f32_16x16x32_bf16 v[64:67], v[166:169], v[196:199], v[64:67]
	v_mfma_f32_16x16x32_bf16 v[52:55], v[146:149], v[204:207], v[52:55]
	v_mfma_f32_16x16x32_bf16 v[48:51], v[166:169], v[204:207], v[48:51]
	v_mfma_f32_16x16x32_bf16 v[36:39], v[146:149], v[218:221], v[36:39]
	v_mfma_f32_16x16x32_bf16 v[32:35], v[166:169], v[218:221], v[32:35]
	v_mfma_f32_16x16x32_bf16 v[18:21], v[146:149], v[230:233], v[18:21]
	v_mfma_f32_16x16x32_bf16 v[14:17], v[166:169], v[230:233], v[14:17]
	s_setprio 0
	s_setprio 1
	v_mfma_f32_16x16x32_bf16 v[60:63], v[170:173], v[192:195], v[60:63]
	v_mfma_f32_16x16x32_bf16 v[56:59], v[184:187], v[192:195], v[56:59]
	v_mfma_f32_16x16x32_bf16 v[44:47], v[170:173], v[200:203], v[44:47]
	v_mfma_f32_16x16x32_bf16 v[40:43], v[184:187], v[200:203], v[40:43]
	v_mfma_f32_16x16x32_bf16 v[28:31], v[170:173], v[208:211], v[28:31]
	v_mfma_f32_16x16x32_bf16 v[24:27], v[184:187], v[208:211], v[24:27]
	v_mfma_f32_16x16x32_bf16 v[10:13], v[170:173], v[226:229], v[10:13]
	v_mfma_f32_16x16x32_bf16 v[6:9], v[184:187], v[226:229], v[6:9]
	v_mfma_f32_16x16x32_bf16 v[60:63], v[174:177], v[196:199], v[60:63]
	v_mfma_f32_16x16x32_bf16 v[56:59], v[188:191], v[196:199], v[56:59]
	v_mfma_f32_16x16x32_bf16 v[44:47], v[174:177], v[204:207], v[44:47]
	v_mfma_f32_16x16x32_bf16 v[40:43], v[188:191], v[204:207], v[40:43]
	v_mfma_f32_16x16x32_bf16 v[28:31], v[174:177], v[218:221], v[28:31]
	v_mfma_f32_16x16x32_bf16 v[24:27], v[188:191], v[218:221], v[24:27]
	v_mfma_f32_16x16x32_bf16 v[10:13], v[174:177], v[230:233], v[10:13]
	v_mfma_f32_16x16x32_bf16 v[6:9], v[188:191], v[230:233], v[6:9]
	s_setprio 0
	s_barrier
	s_add_i32 s22, 0, 0x18000
	v_add_u32_e32 v98, s22, v162
	s_add_i32 s28, 0, 0x1c000
	ds_read_b128 v[142:145], v98
	ds_read_b128 v[146:149], v98 offset:1024
	ds_read_b128 v[150:153], v98 offset:2048
	ds_read_b128 v[166:169], v98 offset:3072
	v_add_u32_e32 v98, s28, v162
	ds_read_b128 v[170:173], v98
	ds_read_b128 v[174:177], v98 offset:1024
	ds_read_b128 v[184:187], v98 offset:2048
	ds_read_b128 v[188:191], v98 offset:3072
	s_add_u32 s40, s40, 0x40000
	s_addc_u32 s41, s41, 0
	s_mov_b32 m0, s52
	v_lshl_add_u64 v[212:213], s[40:41], 0, v[96:97]
	ds_read_b128 v[192:195], v165 offset:32768
	ds_read_b128 v[196:199], v165 offset:33792
	ds_read_b128 v[200:203], v165 offset:34816
	ds_read_b128 v[204:207], v165 offset:35840
	ds_read_b128 v[208:211], v165 offset:36864
	ds_read_b128 v[218:221], v165 offset:37888
	ds_read_b128 v[226:229], v165 offset:38912
	ds_read_b128 v[230:233], v165 offset:39936
	global_load_lds_dwordx4 v[212:213], off
	v_lshl_add_u64 v[212:213], s[40:41], 0, v[156:157]
	s_mov_b32 m0, s53
	s_nop 0
	global_load_lds_dwordx4 v[212:213], off
	s_waitcnt vmcnt(8)
	s_waitcnt lgkmcnt(0)
	s_barrier
	s_setprio 1
	s_waitcnt lgkmcnt(0)
	v_mfma_f32_16x16x32_bf16 v[136:139], v[142:145], v[192:195], v[136:139]
	v_mfma_f32_16x16x32_bf16 v[132:135], v[150:153], v[192:195], v[132:135]
	v_mfma_f32_16x16x32_bf16 v[120:123], v[142:145], v[200:203], v[120:123]
	v_mfma_f32_16x16x32_bf16 v[116:119], v[150:153], v[200:203], v[116:119]
	v_mfma_f32_16x16x32_bf16 v[104:107], v[142:145], v[208:211], v[104:107]
	v_mfma_f32_16x16x32_bf16 v[100:103], v[150:153], v[208:211], v[100:103]
	v_mfma_f32_16x16x32_bf16 v[84:87], v[142:145], v[226:229], v[84:87]
	v_mfma_f32_16x16x32_bf16 v[80:83], v[150:153], v[226:229], v[80:83]
	v_mfma_f32_16x16x32_bf16 v[136:139], v[146:149], v[196:199], v[136:139]
	v_mfma_f32_16x16x32_bf16 v[132:135], v[166:169], v[196:199], v[132:135]
	v_mfma_f32_16x16x32_bf16 v[120:123], v[146:149], v[204:207], v[120:123]
	v_mfma_f32_16x16x32_bf16 v[116:119], v[166:169], v[204:207], v[116:119]
	v_mfma_f32_16x16x32_bf16 v[104:107], v[146:149], v[218:221], v[104:107]
	v_mfma_f32_16x16x32_bf16 v[100:103], v[166:169], v[218:221], v[100:103]
	v_mfma_f32_16x16x32_bf16 v[84:87], v[146:149], v[230:233], v[84:87]
	v_mfma_f32_16x16x32_bf16 v[80:83], v[166:169], v[230:233], v[80:83]
	s_setprio 0
	s_setprio 1
	v_mfma_f32_16x16x32_bf16 v[128:131], v[170:173], v[192:195], v[128:131]
	v_mfma_f32_16x16x32_bf16 v[124:127], v[184:187], v[192:195], v[124:127]
	v_mfma_f32_16x16x32_bf16 v[112:115], v[170:173], v[200:203], v[112:115]
	v_mfma_f32_16x16x32_bf16 v[108:111], v[184:187], v[200:203], v[108:111]
	v_mfma_f32_16x16x32_bf16 v[92:95], v[170:173], v[208:211], v[92:95]
	v_mfma_f32_16x16x32_bf16 v[88:91], v[184:187], v[208:211], v[88:91]
	v_mfma_f32_16x16x32_bf16 v[76:79], v[170:173], v[226:229], v[76:79]
	v_mfma_f32_16x16x32_bf16 v[72:75], v[184:187], v[226:229], v[72:75]
	v_mfma_f32_16x16x32_bf16 v[128:131], v[174:177], v[196:199], v[128:131]
	v_mfma_f32_16x16x32_bf16 v[124:127], v[188:191], v[196:199], v[124:127]
	v_mfma_f32_16x16x32_bf16 v[112:115], v[174:177], v[204:207], v[112:115]
	v_mfma_f32_16x16x32_bf16 v[108:111], v[188:191], v[204:207], v[108:111]
	v_mfma_f32_16x16x32_bf16 v[92:95], v[174:177], v[218:221], v[92:95]
	v_mfma_f32_16x16x32_bf16 v[88:91], v[188:191], v[218:221], v[88:91]
	v_mfma_f32_16x16x32_bf16 v[76:79], v[174:177], v[230:233], v[76:79]
	v_mfma_f32_16x16x32_bf16 v[72:75], v[188:191], v[230:233], v[72:75]
	s_setprio 0
	s_barrier
	s_add_i32 s22, s22, s24
	v_lshl_add_u64 v[154:155], v[154:155], 0, s[0:1]
	s_mov_b32 m0, s22
	ds_read_b128 v[192:195], v165 offset:49152
	ds_read_b128 v[196:199], v165 offset:50176
	ds_read_b128 v[200:203], v165 offset:51200
	ds_read_b128 v[204:207], v165 offset:52224
	ds_read_b128 v[208:211], v165 offset:53248
	ds_read_b128 v[218:221], v165 offset:54272
	ds_read_b128 v[226:229], v165 offset:55296
	ds_read_b128 v[230:233], v165 offset:56320
	global_load_lds_dwordx4 v[154:155], off
	s_add_i32 m0, s22, 0x2000
	s_add_u32 s40, s44, 0x40080
	v_lshl_add_u64 v[154:155], v[178:179], 0, s[0:1]
	s_addc_u32 s41, s45, 0
	s_add_i32 s22, s28, s24
	global_load_lds_dwordx4 v[154:155], off
	v_lshl_add_u64 v[154:155], s[40:41], 0, v[96:97]
	s_mov_b32 m0, s22
	s_nop 0
	global_load_lds_dwordx4 v[154:155], off
	v_lshl_add_u64 v[154:155], s[40:41], 0, v[156:157]
	s_add_i32 m0, s22, 0x2000
	s_nop 0
	global_load_lds_dwordx4 v[154:155], off
	v_lshl_add_u64 v[154:155], v[180:181], 0, s[0:1]
	s_mov_b32 m0, s4
	s_nop 0
	global_load_lds_dwordx4 v[154:155], off
	v_lshl_add_u64 v[154:155], v[182:183], 0, s[0:1]
	s_mov_b32 m0, s54
	s_nop 0
	global_load_lds_dwordx4 v[154:155], off
	s_waitcnt vmcnt(8)
	s_waitcnt lgkmcnt(0)
	s_barrier
	s_setprio 1
	s_waitcnt lgkmcnt(0)
	v_mfma_f32_16x16x32_bf16 v[68:71], v[142:145], v[192:195], v[68:71]
	v_mfma_f32_16x16x32_bf16 v[64:67], v[150:153], v[192:195], v[64:67]
	v_mfma_f32_16x16x32_bf16 v[52:55], v[142:145], v[200:203], v[52:55]
	v_mfma_f32_16x16x32_bf16 v[48:51], v[150:153], v[200:203], v[48:51]
	v_mfma_f32_16x16x32_bf16 v[36:39], v[142:145], v[208:211], v[36:39]
	v_mfma_f32_16x16x32_bf16 v[32:35], v[150:153], v[208:211], v[32:35]
	v_mfma_f32_16x16x32_bf16 v[18:21], v[142:145], v[226:229], v[18:21]
	v_mfma_f32_16x16x32_bf16 v[14:17], v[150:153], v[226:229], v[14:17]
	v_mfma_f32_16x16x32_bf16 v[68:71], v[146:149], v[196:199], v[68:71]
	v_mfma_f32_16x16x32_bf16 v[64:67], v[166:169], v[196:199], v[64:67]
	v_mfma_f32_16x16x32_bf16 v[52:55], v[146:149], v[204:207], v[52:55]
	v_mfma_f32_16x16x32_bf16 v[48:51], v[166:169], v[204:207], v[48:51]
	v_mfma_f32_16x16x32_bf16 v[36:39], v[146:149], v[218:221], v[36:39]
	v_mfma_f32_16x16x32_bf16 v[32:35], v[166:169], v[218:221], v[32:35]
	v_mfma_f32_16x16x32_bf16 v[18:21], v[146:149], v[230:233], v[18:21]
	v_mfma_f32_16x16x32_bf16 v[14:17], v[166:169], v[230:233], v[14:17]
	s_setprio 0
	s_setprio 1
	v_mfma_f32_16x16x32_bf16 v[60:63], v[170:173], v[192:195], v[60:63]
	v_mfma_f32_16x16x32_bf16 v[56:59], v[184:187], v[192:195], v[56:59]
	v_mfma_f32_16x16x32_bf16 v[44:47], v[170:173], v[200:203], v[44:47]
	v_mfma_f32_16x16x32_bf16 v[40:43], v[184:187], v[200:203], v[40:43]
	v_mfma_f32_16x16x32_bf16 v[28:31], v[170:173], v[208:211], v[28:31]
	v_mfma_f32_16x16x32_bf16 v[24:27], v[184:187], v[208:211], v[24:27]
	v_mfma_f32_16x16x32_bf16 v[10:13], v[170:173], v[226:229], v[10:13]
	v_mfma_f32_16x16x32_bf16 v[6:9], v[184:187], v[226:229], v[6:9]
	v_mfma_f32_16x16x32_bf16 v[60:63], v[174:177], v[196:199], v[60:63]
	v_mfma_f32_16x16x32_bf16 v[56:59], v[188:191], v[196:199], v[56:59]
	v_mfma_f32_16x16x32_bf16 v[44:47], v[174:177], v[204:207], v[44:47]
	v_mfma_f32_16x16x32_bf16 v[40:43], v[188:191], v[204:207], v[40:43]
	v_mfma_f32_16x16x32_bf16 v[28:31], v[174:177], v[218:221], v[28:31]
	v_mfma_f32_16x16x32_bf16 v[24:27], v[188:191], v[218:221], v[24:27]
	v_mfma_f32_16x16x32_bf16 v[10:13], v[174:177], v[230:233], v[10:13]
	v_mfma_f32_16x16x32_bf16 v[6:9], v[188:191], v[230:233], v[6:9]
	s_setprio 0
	s_barrier
	s_mov_b32 s100, 0
	s_add_i32 s78, s78, 2
	s_cmp_gt_u32 s78, 13
	s_mov_b64 s[40:41], s[42:43]
	s_cbranch_scc0 .LBB0_2958
	s_and_b64 vcc, exec, s[14:15]
	s_cbranch_vccz .LBB0_2961
	s_barrier

	.amdhsa_kernel _ZN2mk4megaENS_4ArgsE
		.amdhsa_group_segment_fixed_size 0
		.amdhsa_private_segment_fixed_size 0
		.amdhsa_kernarg_size 544
		.amdhsa_user_sgpr_count 2
		.amdhsa_user_sgpr_dispatch_ptr 0
		.amdhsa_user_sgpr_queue_ptr 0
		.amdhsa_user_sgpr_kernarg_segment_ptr 1
		.amdhsa_user_sgpr_dispatch_id 0
		.amdhsa_user_sgpr_kernarg_preload_length 0
		.amdhsa_user_sgpr_kernarg_preload_offset 0
		.amdhsa_user_sgpr_private_segment_size 0
		.amdhsa_uses_dynamic_stack 0
		.amdhsa_enable_private_segment 0
		.amdhsa_system_sgpr_workgroup_id_x 1
		.amdhsa_system_sgpr_workgroup_id_y 0
		.amdhsa_system_sgpr_workgroup_id_z 0
		.amdhsa_system_sgpr_workgroup_info 0
		.amdhsa_system_vgpr_workitem_id 0
		.amdhsa_next_free_vgpr 256
		.amdhsa_next_free_sgpr 102
		.amdhsa_accum_offset 256
		.amdhsa_reserve_vcc 1
		.amdhsa_float_round_mode_32 0
		.amdhsa_float_round_mode_16_64 0
		.amdhsa_float_denorm_mode_32 3
		.amdhsa_float_denorm_mode_16_64 3
		.amdhsa_dx10_clamp 1
		.amdhsa_ieee_mode 1
		.amdhsa_fp16_overflow 0
		.amdhsa_tg_split 0
		.amdhsa_exception_fp_ieee_invalid_op 0
		.amdhsa_exception_fp_denorm_src 0
		.amdhsa_exception_fp_ieee_div_zero 0
		.amdhsa_exception_fp_ieee_overflow 0
		.amdhsa_exception_fp_ieee_underflow 0
		.amdhsa_exception_fp_ieee_inexact 0
		.amdhsa_exception_int_div_zero 0
	.end_amdhsa_kernel

amdhsa.kernels:
  - .agpr_count:     0
    .args:
      - .offset:         0
        .size:           288
        .value_kind:     by_value
      - .offset:         288
        .size:           4
        .value_kind:     hidden_block_count_x
      - .offset:         292
        .size:           4
        .value_kind:     hidden_block_count_y
      - .offset:         296
        .size:           4
        .value_kind:     hidden_block_count_z
      - .offset:         300
        .size:           2
        .value_kind:     hidden_group_size_x
      - .offset:         302
        .size:           2
        .value_kind:     hidden_group_size_y
      - .offset:         304
        .size:           2
        .value_kind:     hidden_group_size_z
      - .offset:         306
        .size:           2
        .value_kind:     hidden_remainder_x
      - .offset:         308
        .size:           2
        .value_kind:     hidden_remainder_y
      - .offset:         310
        .size:           2
        .value_kind:     hidden_remainder_z
      - .offset:         328
        .size:           8
        .value_kind:     hidden_global_offset_x
      - .offset:         336
        .size:           8
        .value_kind:     hidden_global_offset_y
      - .offset:         344
        .size:           8
        .value_kind:     hidden_global_offset_z
      - .offset:         352
        .size:           2
        .value_kind:     hidden_grid_dims
      - .offset:         408
        .size:           4
        .value_kind:     hidden_dynamic_lds_size
    .group_segment_fixed_size: 0
    .kernarg_segment_align: 8
    .kernarg_segment_size: 544
    .language:       OpenCL C
    .language_version:
      - 2
      - 0
    .max_flat_workgroup_size: 512
    .name:           _ZN2mk4megaENS_4ArgsE
    .private_segment_fixed_size: 0
    .sgpr_count:     108
    .sgpr_spill_count: 319
    .symbol:         _ZN2mk4megaENS_4ArgsE.kd
    .uniform_work_group_size: 1
    .uses_dynamic_stack: false
    .vgpr_count:     256
    .vgpr_spill_count: 0
    .wavefront_size: 64
